# baseline (speedup 1.0000x reference)
.LBB1_8:
	s_or_b64 exec, exec, s[4:5]
	v_add_u32_e32 v10, v172, v2
	s_waitcnt vmcnt(1) lgkmcnt(0)
	s_barrier
	s_nop 0
	s_nop 0
	ds_read_b128 v[18:21], v10 offset:256
	ds_read_b128 v[22:25], v10 offset:288
	ds_read_b128 v[82:85], v10 offset:320
	ds_read_b128 v[86:89], v10 offset:352
	ds_read_b128 v[74:77], v10 offset:384
	ds_read_b128 v[78:81], v10 offset:416
	ds_read_b128 v[2:5], v213 offset:32768
	ds_read_b128 v[6:9], v213 offset:0
	ds_read_b128 v[66:69], v10 offset:448
	ds_read_b128 v[70:73], v10 offset:480
	ds_read_b128 v[10:13], v213 offset:1024
	s_waitcnt lgkmcnt(3)
	v_pk_mul_f32 v[26:27], v[8:9], v[20:21]
	v_pk_mul_f32 v[28:29], v[6:7], v[18:19]
	ds_read_b128 v[14:17], v213 offset:8192
	s_waitcnt lgkmcnt(1)
	v_pk_mul_f32 v[12:13], v[12:13], v[24:25]
	v_pk_mul_f32 v[10:11], v[10:11], v[22:23]
	v_pk_fma_f32 v[30:31], v[8:9], v[20:21], v[12:13]
	v_pk_fma_f32 v[32:33], v[6:7], v[18:19], v[10:11]
	v_cvt_pk_bf16_f32 v9, v12, v13
	v_cvt_pk_bf16_f32 v7, v26, v27
	v_cvt_pk_bf16_f32 v8, v10, v11
	v_cvt_pk_bf16_f32 v6, v28, v29
	ds_read_b128 v[10:13], v213 offset:33792
	s_nop 0
	v_mfma_f32_32x32x16_bf16 v[34:49], v[2:5], v[6:9], 0
	ds_read_b128 v[6:9], v213 offset:9216
	s_waitcnt lgkmcnt(2)
	v_mul_f32_e32 v26, v16, v20
	v_mul_f32_e32 v27, v17, v21
	v_pk_mul_f32 v[50:51], v[14:15], v[18:19]
	s_mov_b32 s4, 0x3727c5ac
	s_waitcnt lgkmcnt(0)
	v_pk_mul_f32 v[8:9], v[8:9], v[24:25]
	v_pk_mul_f32 v[28:29], v[6:7], v[22:23]
	v_pk_fma_f32 v[90:91], v[16:17], v[20:21], v[8:9]
	v_pk_fma_f32 v[92:93], v[14:15], v[18:19], v[28:29]
	ds_read_b128 v[14:17], v213 offset:2048
	v_cvt_pk_bf16_f32 v9, v8, v9
	v_cvt_pk_bf16_f32 v7, v26, v27
	v_cvt_pk_bf16_f32 v8, v28, v29
	ds_read_b128 v[26:29], v213 offset:3072
	v_cvt_pk_bf16_f32 v6, v50, v51
	s_waitcnt lgkmcnt(1)
	v_pk_mul_f32 v[94:95], v[14:15], v[82:83]
	s_mov_b32 s0, 0x3c800000
	v_mfma_f32_32x32x16_bf16 v[50:65], v[2:5], v[6:9], 0
	v_mul_f32_e32 v2, v16, v84
	v_mul_f32_e32 v3, v17, v85
	s_waitcnt lgkmcnt(0)
	v_mul_f32_e32 v4, v28, v88
	v_mul_f32_e32 v5, v29, v89
	v_pk_mul_f32 v[6:7], v[26:27], v[86:87]
	v_pk_fma_f32 v[8:9], v[16:17], v[84:85], v[4:5]
	v_cvt_pk_bf16_f32 v3, v2, v3
	v_pk_fma_f32 v[14:15], v[14:15], v[82:83], v[6:7]
	v_pk_add_f32 v[26:27], v[8:9], v[30:31]
	v_cvt_pk_bf16_f32 v5, v4, v5
	v_cvt_pk_bf16_f32 v4, v6, v7
	ds_read_b128 v[6:9], v213 offset:10240
	v_pk_add_f32 v[28:29], v[14:15], v[32:33]
	ds_read_b128 v[14:17], v213 offset:11264
	v_cvt_pk_bf16_f32 v2, v94, v95
	s_waitcnt lgkmcnt(1)
	v_pk_mul_f32 v[30:31], v[6:7], v[82:83]
	v_mov_b64_e32 v[152:153], s[4:5]
	v_mfma_f32_32x32x16_bf16 v[34:49], v[10:13], v[2:5], v[34:49]
	v_mul_f32_e32 v2, v8, v84
	v_mul_f32_e32 v3, v9, v85
	s_waitcnt lgkmcnt(0)
	v_mul_f32_e32 v4, v16, v88
	v_mul_f32_e32 v5, v17, v89
	v_pk_mul_f32 v[14:15], v[14:15], v[86:87]
	v_pk_fma_f32 v[8:9], v[8:9], v[84:85], v[4:5]
	v_pk_fma_f32 v[6:7], v[6:7], v[82:83], v[14:15]
	v_cvt_pk_bf16_f32 v5, v4, v5
	v_cvt_pk_bf16_f32 v3, v2, v3
	v_cvt_pk_bf16_f32 v4, v14, v15
	v_pk_add_f32 v[32:33], v[8:9], v[90:91]
	v_pk_add_f32 v[90:91], v[6:7], v[92:93]
	ds_read_b128 v[6:9], v213 offset:34816
	ds_read_b128 v[14:17], v213 offset:4096
	v_cvt_pk_bf16_f32 v2, v30, v31
	s_mov_b32 s13, 0
	s_mov_b64 s[6:7], 0
	v_mfma_f32_32x32x16_bf16 v[50:65], v[10:13], v[2:5], v[50:65]
	ds_read_b128 v[2:5], v213 offset:5120
	ds_read_b128 v[10:13], v213 offset:12288
	s_waitcnt lgkmcnt(2)
	v_pk_mul_f32 v[30:31], v[16:17], v[76:77]
	v_pk_mul_f32 v[92:93], v[14:15], v[74:75]
	s_waitcnt lgkmcnt(1)
	v_pk_mul_f32 v[4:5], v[4:5], v[80:81]
	v_pk_mul_f32 v[94:95], v[2:3], v[78:79]
	v_pk_fma_f32 v[2:3], v[16:17], v[76:77], v[4:5]
	v_cvt_pk_bf16_f32 v5, v4, v5
	v_pk_add_f32 v[96:97], v[2:3], v[26:27]
	v_cvt_pk_bf16_f32 v3, v30, v31
	v_cvt_pk_bf16_f32 v4, v94, v95
	v_cvt_pk_bf16_f32 v2, v92, v93
	v_pk_fma_f32 v[14:15], v[14:15], v[74:75], v[94:95]
	s_waitcnt lgkmcnt(0)
	v_pk_mul_f32 v[30:31], v[10:11], v[74:75]
	v_mfma_f32_32x32x16_bf16 v[34:49], v[6:9], v[2:5], v[34:49]
	ds_read_b128 v[2:5], v213 offset:13312
	v_add_f32_e32 v98, v14, v28
	v_add_f32_e32 v99, v15, v29
	ds_read_b128 v[14:17], v213 offset:35840
	v_pk_mul_f32 v[26:27], v[12:13], v[76:77]
	s_waitcnt lgkmcnt(1)
	v_pk_mul_f32 v[4:5], v[4:5], v[80:81]
	v_pk_mul_f32 v[28:29], v[2:3], v[78:79]
	v_pk_fma_f32 v[2:3], v[12:13], v[76:77], v[4:5]
	v_pk_fma_f32 v[10:11], v[10:11], v[74:75], v[28:29]
	v_pk_add_f32 v[32:33], v[2:3], v[32:33]
	v_pk_add_f32 v[92:93], v[10:11], v[90:91]
	ds_read_b128 v[10:13], v213 offset:6144
	v_cvt_pk_bf16_f32 v5, v4, v5
	v_cvt_pk_bf16_f32 v3, v26, v27
	v_cvt_pk_bf16_f32 v4, v28, v29
	ds_read_b128 v[26:29], v213 offset:7168
	v_cvt_pk_bf16_f32 v2, v30, v31
	s_waitcnt lgkmcnt(1)
	v_pk_mul_f32 v[30:31], v[10:11], v[66:67]
	v_mfma_f32_32x32x16_bf16 v[50:65], v[6:9], v[2:5], v[50:65]
	v_mul_f32_e32 v2, v12, v68
	v_mul_f32_e32 v3, v13, v69
	s_waitcnt lgkmcnt(0)
	v_mul_f32_e32 v4, v28, v72
	v_mul_f32_e32 v5, v29, v73
	v_pk_mul_f32 v[6:7], v[26:27], v[70:71]
	v_pk_fma_f32 v[8:9], v[12:13], v[68:69], v[4:5]
	v_cvt_pk_bf16_f32 v3, v2, v3
	v_pk_fma_f32 v[10:11], v[10:11], v[66:67], v[6:7]
	v_pk_add_f32 v[94:95], v[8:9], v[96:97]
	v_cvt_pk_bf16_f32 v5, v4, v5
	v_cvt_pk_bf16_f32 v4, v6, v7
	ds_read_b128 v[6:9], v213 offset:14336
	v_pk_add_f32 v[96:97], v[10:11], v[98:99]
	ds_read_b128 v[10:13], v213 offset:15360
	v_cvt_pk_bf16_f32 v2, v30, v31
	s_waitcnt lgkmcnt(1)
	v_pk_mul_f32 v[30:31], v[6:7], v[66:67]
	v_mfma_f32_32x32x16_bf16 v[34:49], v[14:17], v[2:5], v[34:49]
	s_waitcnt lgkmcnt(0)
	v_mul_f32_e32 v10, v10, v70
	v_mul_f32_e32 v11, v11, v71
	v_mul_f32_e32 v2, v8, v68
	v_mul_f32_e32 v3, v9, v69
	v_pk_mul_f32 v[4:5], v[12:13], v[72:73]
	v_pk_fma_f32 v[6:7], v[6:7], v[66:67], v[10:11]
	v_pk_fma_f32 v[8:9], v[8:9], v[68:69], v[4:5]
	v_pk_add_f32 v[92:93], v[6:7], v[92:93]
	v_cvt_pk_bf16_f32 v3, v2, v3
	v_pk_add_f32 v[90:91], v[8:9], v[32:33]
	v_cvt_pk_bf16_f32 v5, v4, v5
	v_cvt_pk_bf16_f32 v4, v10, v11
	ds_read_b128 v[26:29], v213 offset:36864
	ds_read_b128 v[6:9], v213 offset:16384
	v_cvt_pk_bf16_f32 v2, v30, v31
	ds_read_b128 v[98:101], v213 offset:25600
	ds_read_b128 v[102:105], v213 offset:37888
	v_mfma_f32_32x32x16_bf16 v[50:65], v[14:17], v[2:5], v[50:65]
	ds_read_b128 v[2:5], v213 offset:17408
	ds_read_b128 v[30:33], v213 offset:24576
	s_waitcnt lgkmcnt(4)
	v_pk_mul_f32 v[12:13], v[6:7], v[18:19]
	v_pk_mul_f32 v[10:11], v[8:9], v[20:21]
	s_waitcnt lgkmcnt(1)
	v_pk_mul_f32 v[14:15], v[2:3], v[22:23]
	v_pk_mul_f32 v[22:23], v[98:99], v[22:23]
	v_pk_fma_f32 v[112:113], v[6:7], v[18:19], v[14:15]
	s_waitcnt lgkmcnt(0)
	v_pk_mul_f32 v[114:115], v[30:31], v[18:19]
	v_pk_fma_f32 v[118:119], v[30:31], v[18:19], v[22:23]
	v_pk_mul_f32 v[4:5], v[4:5], v[24:25]
	v_pk_mul_f32 v[106:107], v[32:33], v[20:21]
	v_pk_mul_f32 v[24:25], v[100:101], v[24:25]
	ds_read_b128 v[98:101], v213 offset:18432
	v_cvt_pk_bf16_f32 v19, v106, v107
	ds_read_b128 v[106:109], v213 offset:19456
	v_pk_fma_f32 v[110:111], v[8:9], v[20:21], v[4:5]
	v_cvt_pk_bf16_f32 v5, v4, v5
	v_cvt_pk_bf16_f32 v3, v10, v11
	v_cvt_pk_bf16_f32 v4, v14, v15
	s_waitcnt lgkmcnt(0)
	v_pk_mul_f32 v[106:107], v[106:107], v[86:87]
	v_cvt_pk_bf16_f32 v2, v12, v13
	v_pk_mul_f32 v[120:121], v[98:99], v[82:83]
	v_pk_mul_f32 v[108:109], v[108:109], v[88:89]
	v_pk_fma_f32 v[98:99], v[98:99], v[82:83], v[106:107]
	v_mfma_f32_32x32x16_bf16 v[2:17], v[26:29], v[2:5], 0
	v_cvt_pk_bf16_f32 v18, v114, v115
	v_mul_f32_e32 v114, v100, v84
	v_mul_f32_e32 v115, v101, v85
	v_fma_f32 v100, v100, v84, v108
	v_fma_f32 v101, v101, v85, v109
	v_pk_add_f32 v[124:125], v[98:99], v[112:113]
	v_pk_add_f32 v[122:123], v[100:101], v[110:111]
	v_cvt_pk_bf16_f32 v101, v108, v109
	v_cvt_pk_bf16_f32 v100, v106, v107
	ds_read_b128 v[106:109], v213 offset:26624
	v_pk_fma_f32 v[116:117], v[32:33], v[20:21], v[24:25]
	v_cvt_pk_bf16_f32 v21, v24, v25
	v_cvt_pk_bf16_f32 v20, v22, v23
	ds_read_b128 v[110:113], v213 offset:27648
	v_cvt_pk_bf16_f32 v99, v114, v115
	v_mfma_f32_32x32x16_bf16 v[18:33], v[26:29], v[18:21], 0
	v_cvt_pk_bf16_f32 v98, v120, v121
	s_waitcnt lgkmcnt(1)
	v_mul_f32_e32 v114, v106, v82
	v_mul_f32_e32 v115, v107, v83
	s_waitcnt lgkmcnt(0)
	v_pk_mul_f32 v[86:87], v[110:111], v[86:87]
	v_pk_mul_f32 v[88:89], v[112:113], v[88:89]
	v_pk_fma_f32 v[82:83], v[106:107], v[82:83], v[86:87]
	v_mfma_f32_32x32x16_bf16 v[2:17], v[102:105], v[98:101], v[2:17]
	v_mul_f32_e32 v98, v108, v84
	v_mul_f32_e32 v99, v109, v85
	v_fma_f32 v84, v108, v84, v88
	v_fma_f32 v85, v109, v85, v89
	v_add_f32_e32 v108, v82, v118
	v_add_f32_e32 v109, v83, v119
	v_cvt_pk_bf16_f32 v83, v98, v99
	v_pk_add_f32 v[106:107], v[84:85], v[116:117]
	v_cvt_pk_bf16_f32 v85, v88, v89
	v_cvt_pk_bf16_f32 v84, v86, v87
	ds_read_b128 v[86:89], v213 offset:38912
	ds_read_b128 v[98:101], v213 offset:20480
	v_cvt_pk_bf16_f32 v82, v114, v115
	s_waitcnt lgkmcnt(0)
	v_pk_mul_f32 v[110:111], v[100:101], v[76:77]
	v_mfma_f32_32x32x16_bf16 v[18:33], v[102:105], v[82:85], v[18:33]
	ds_read_b128 v[82:85], v213 offset:21504
	ds_read_b128 v[102:105], v213 offset:28672
	v_mul_f32_e32 v112, v98, v74
	v_mul_f32_e32 v113, v99, v75
	s_waitcnt lgkmcnt(1)
	v_pk_mul_f32 v[84:85], v[84:85], v[80:81]
	v_pk_mul_f32 v[114:115], v[82:83], v[78:79]
	v_pk_fma_f32 v[82:83], v[100:101], v[76:77], v[84:85]
	v_cvt_pk_bf16_f32 v85, v84, v85
	v_pk_add_f32 v[116:117], v[82:83], v[122:123]
	v_cvt_pk_bf16_f32 v83, v110, v111
	v_cvt_pk_bf16_f32 v84, v114, v115
	v_cvt_pk_bf16_f32 v82, v112, v113
	v_pk_fma_f32 v[98:99], v[98:99], v[74:75], v[114:115]
	s_waitcnt lgkmcnt(0)
	v_pk_mul_f32 v[112:113], v[102:103], v[74:75]
	v_mfma_f32_32x32x16_bf16 v[2:17], v[86:89], v[82:85], v[2:17]
	ds_read_b128 v[82:85], v213 offset:29696
	v_add_f32_e32 v118, v98, v124
	v_add_f32_e32 v119, v99, v125
	v_mul_f32_e32 v110, v104, v76
	v_mul_f32_e32 v111, v105, v77
	ds_read_b128 v[98:101], v213 offset:39936
	s_waitcnt lgkmcnt(1)
	v_pk_mul_f32 v[78:79], v[82:83], v[78:79]
	v_pk_mul_f32 v[80:81], v[84:85], v[80:81]
	v_pk_fma_f32 v[74:75], v[102:103], v[74:75], v[78:79]
	v_pk_fma_f32 v[76:77], v[104:105], v[76:77], v[80:81]
	v_pk_add_f32 v[104:105], v[74:75], v[108:109]
	v_pk_add_f32 v[102:103], v[76:77], v[106:107]
	v_cvt_pk_bf16_f32 v77, v80, v81
	v_cvt_pk_bf16_f32 v76, v78, v79
	ds_read_b128 v[78:81], v213 offset:22528
	ds_read_b128 v[82:85], v213 offset:23552
	v_cvt_pk_bf16_f32 v75, v110, v111
	v_cvt_pk_bf16_f32 v74, v112, v113
	s_waitcnt lgkmcnt(0)
	v_pk_mul_f32 v[82:83], v[82:83], v[70:71]
	v_mfma_f32_32x32x16_bf16 v[18:33], v[86:89], v[74:77], v[18:33]
	v_mul_f32_e32 v74, v80, v68
	v_mul_f32_e32 v75, v81, v69
	v_mul_f32_e32 v76, v84, v72
	v_mul_f32_e32 v77, v85, v73
	v_mul_f32_e32 v86, v78, v66
	v_mul_f32_e32 v87, v79, v67
	v_pk_fma_f32 v[80:81], v[80:81], v[68:69], v[76:77]
	v_pk_fma_f32 v[78:79], v[78:79], v[66:67], v[82:83]
	v_cvt_pk_bf16_f32 v75, v74, v75
	v_pk_add_f32 v[88:89], v[80:81], v[116:117]
	v_pk_add_f32 v[106:107], v[78:79], v[118:119]
	ds_read_b128 v[78:81], v213 offset:30720
	v_cvt_pk_bf16_f32 v77, v76, v77
	v_cvt_pk_bf16_f32 v76, v82, v83
	ds_read_b128 v[82:85], v213 offset:31744
	v_cvt_pk_bf16_f32 v74, v86, v87
	s_waitcnt lgkmcnt(0)
	v_pk_mul_f32 v[72:73], v[84:85], v[72:73]
	v_mfma_f32_32x32x16_bf16 v[2:17], v[98:101], v[74:77], v[2:17]
	v_mul_f32_e32 v74, v80, v68
	v_mul_f32_e32 v75, v81, v69
	v_fma_f32 v68, v80, v68, v72
	v_fma_f32 v69, v81, v69, v73
	v_mul_f32_e32 v70, v82, v70
	v_mul_f32_e32 v71, v83, v71
	v_pk_add_f32 v[84:85], v[68:69], v[102:103]
	v_cvt_pk_bf16_f32 v69, v72, v73
	v_pk_mov_b32 v[72:73], v[96:97], v[94:95] op_sel:[1,0]
	v_mov_b32_e32 v97, v95
	v_pk_add_f32 v[72:73], v[72:73], v[96:97]
	v_pk_mul_f32 v[76:77], v[78:79], v[66:67]
	v_pk_fma_f32 v[66:67], v[78:79], v[66:67], v[70:71]
	v_pk_add_f32 v[72:73], v[72:73], v[72:73] op_sel:[0,1] op_sel_hi:[1,0]
	v_pk_add_f32 v[86:87], v[66:67], v[104:105]
	v_mov_b32_e32 v66, v72
	s_nop 1
	v_permlane32_swap_b32_e32 v72, v66
	v_add_f32_e32 v66, v72, v66
	v_cvt_pk_bf16_f32 v67, v74, v75
	v_rcp_f32_e32 v74, v66
	v_cvt_pk_bf16_f32 v68, v70, v71
	v_cvt_pk_bf16_f32 v66, v76, v77
	v_pk_mul_f32 v[70:71], v[46:47], v[74:75] op_sel_hi:[1,0]
	s_nop 0
	v_mfma_f32_32x32x16_bf16 v[18:33], v[98:101], v[66:69], v[18:33]
	v_mul_f32_e32 v66, v42, v74
	v_mul_f32_e32 v67, v43, v74
	v_pk_mov_b32 v[42:43], v[92:93], v[90:91] op_sel:[1,0]
	v_mov_b32_e32 v93, v91
	v_pk_add_f32 v[42:43], v[42:43], v[92:93]
	v_pk_mul_f32 v[68:69], v[44:45], v[74:75] op_sel_hi:[1,0]
	v_pk_add_f32 v[42:43], v[42:43], v[42:43] op_sel:[0,1] op_sel_hi:[1,0]
	v_pk_mov_b32 v[44:45], v[106:107], v[88:89] op_sel:[1,0]
	v_mov_b32_e32 v43, v42
	s_nop 1
	v_permlane32_swap_b32_e32 v42, v43
	v_add_f32_e32 v42, v42, v43
	v_rcp_f32_e32 v42, v42
	v_mov_b32_e32 v107, v89
	v_pk_add_f32 v[44:45], v[44:45], v[106:107]
	v_pk_mul_f32 v[72:73], v[48:49], v[74:75] op_sel_hi:[1,0]
	v_pk_add_f32 v[44:45], v[44:45], v[44:45] op_sel:[0,1] op_sel_hi:[1,0]
	v_pk_mul_f32 v[36:37], v[36:37], v[74:75] op_sel_hi:[1,0]
	v_pk_mul_f32 v[38:39], v[38:39], v[74:75] op_sel_hi:[1,0]
	v_pk_mul_f32 v[40:41], v[40:41], v[74:75] op_sel_hi:[1,0]
	v_pk_mul_f32 v[34:35], v[34:35], v[74:75] op_sel_hi:[1,0]
	v_pk_mul_f32 v[74:75], v[58:59], v[42:43] op_sel_hi:[1,0]
	v_pk_mul_f32 v[78:79], v[60:61], v[42:43] op_sel_hi:[1,0]
	v_pk_mul_f32 v[80:81], v[62:63], v[42:43] op_sel_hi:[1,0]
	v_pk_mul_f32 v[82:83], v[64:65], v[42:43] op_sel_hi:[1,0]
	v_pk_mul_f32 v[92:93], v[52:53], v[42:43] op_sel_hi:[1,0]
	v_mov_b32_e32 v43, v44
	s_nop 1
	v_permlane32_swap_b32_e32 v44, v43
	v_add_f32_e32 v43, v44, v43
	v_rcp_f32_e32 v76, v43
	v_pk_mul_f32 v[96:97], v[54:55], v[42:43] op_sel_hi:[1,0]
	v_pk_mul_f32 v[94:95], v[56:57], v[42:43] op_sel_hi:[1,0]
	v_pk_mul_f32 v[98:99], v[50:51], v[42:43] op_sel_hi:[1,0]
	v_pk_mul_f32 v[100:101], v[4:5], v[76:77] op_sel_hi:[1,0]
	v_pk_mov_b32 v[4:5], v[86:87], v[84:85] op_sel:[1,0]
	v_mov_b32_e32 v87, v85
	v_pk_add_f32 v[4:5], v[4:5], v[86:87]
	v_pk_mul_f32 v[102:103], v[6:7], v[76:77] op_sel_hi:[1,0]
	v_pk_add_f32 v[104:105], v[4:5], v[4:5] op_sel:[0,1] op_sel_hi:[1,0]
	v_cvt_pk_bf16_f32 v7, v40, v41
	ds_read_b128 v[84:87], v150 offset:52224
	ds_read_b128 v[50:53], v150 offset:35840
	ds_read_b128 v[54:57], v150 offset:36864
	ds_read_b128 v[58:61], v150 offset:37888
	ds_read_b128 v[62:65], v150 offset:38912
	v_cvt_pk_bf16_f32 v6, v38, v39
	v_cvt_pk_bf16_f32 v5, v36, v37
	v_cvt_pk_bf16_f32 v4, v34, v35
	ds_read_b128 v[88:91], v150 offset:53248
	ds_read_b128 v[34:37], v150 offset:39936
	ds_read_b128 v[38:41], v150 offset:40960
	ds_read_b128 v[42:45], v150 offset:41984
	ds_read_b128 v[46:49], v150 offset:43008
	v_cvt_pk_bf16_f32 v95, v94, v95
	v_cvt_pk_bf16_f32 v94, v96, v97
	v_cvt_pk_bf16_f32 v93, v92, v93
	v_cvt_pk_bf16_f32 v92, v98, v99
	s_waitcnt lgkmcnt(5)
	v_mfma_f32_32x32x16_bf16 v[50:65], v[84:87], v[4:7], v[50:65]
	v_mul_f32_e32 v10, v10, v76
	v_mul_f32_e32 v11, v11, v76
	v_mul_f32_e32 v12, v12, v76
	v_mul_f32_e32 v13, v13, v76
	v_mul_f32_e32 v8, v8, v76
	v_mul_f32_e32 v9, v9, v76
	v_mov_b32_e32 v77, v104
	s_nop 1
	v_permlane32_swap_b32_e32 v104, v77
	v_cvt_pk_bf16_f32 v73, v72, v73
	s_waitcnt lgkmcnt(0)
	v_mfma_f32_32x32x16_bf16 v[34:49], v[84:87], v[92:95], v[34:49]
	v_cvt_pk_bf16_f32 v72, v70, v71
	v_cvt_pk_bf16_f32 v70, v66, v67
	v_add_f32_e32 v66, v104, v77
	v_cvt_pk_bf16_f32 v71, v68, v69
	v_rcp_f32_e32 v104, v66
	v_cvt_pk_bf16_f32 v69, v82, v83
	v_cvt_pk_bf16_f32 v68, v80, v81
	v_cvt_pk_bf16_f32 v67, v78, v79
	v_cvt_pk_bf16_f32 v66, v74, v75
	ds_read_b128 v[78:81], v150 offset:54272
	v_mfma_f32_32x32x16_bf16 v[50:65], v[88:91], v[70:73], v[50:65]
	v_mul_f32_e32 v2, v2, v76
	v_mul_f32_e32 v3, v3, v76
	v_mul_f32_e32 v20, v20, v104
	v_mul_f32_e32 v21, v21, v104
	v_cvt_pk_bf16_f32 v85, v8, v9
	v_cvt_pk_bf16_f32 v82, v2, v3
	v_pk_mul_f32 v[2:3], v[22:23], v[104:105] op_sel_hi:[1,0]
	v_pk_mul_f32 v[8:9], v[24:25], v[104:105] op_sel_hi:[1,0]
	v_pk_mul_f32 v[18:19], v[18:19], v[104:105] op_sel_hi:[1,0]
	v_mfma_f32_32x32x16_bf16 v[34:49], v[88:91], v[66:69], v[34:49]
	v_cvt_pk_bf16_f32 v84, v102, v103
	v_cvt_pk_bf16_f32 v83, v100, v101
	ds_read_b128 v[86:89], v150 offset:55296
	v_cvt_pk_bf16_f32 v99, v8, v9
	v_cvt_pk_bf16_f32 v98, v2, v3
	v_cvt_pk_bf16_f32 v97, v20, v21
	v_cvt_pk_bf16_f32 v96, v18, v19
	s_waitcnt lgkmcnt(1)
	v_mfma_f32_32x32x16_bf16 v[50:65], v[78:81], v[82:85], v[50:65]
	v_mul_f32_e32 v2, v14, v76
	v_mul_f32_e32 v3, v15, v76
	v_mul_f32_e32 v8, v16, v76
	v_mul_f32_e32 v9, v17, v76
	v_mul_f32_e32 v14, v26, v104
	v_mul_f32_e32 v15, v27, v104
	v_cvt_pk_bf16_f32 v77, v8, v9
	v_cvt_pk_bf16_f32 v76, v2, v3
	v_cvt_pk_bf16_f32 v74, v10, v11
	v_pk_mul_f32 v[2:3], v[28:29], v[104:105] op_sel_hi:[1,0]
	v_mfma_f32_32x32x16_bf16 v[34:49], v[78:81], v[96:99], v[34:49]
	v_mul_f32_e32 v8, v30, v104
	v_mul_f32_e32 v9, v31, v104
	v_mul_f32_e32 v10, v32, v104
	v_mul_f32_e32 v11, v33, v104
	v_cvt_pk_bf16_f32 v75, v12, v13
	v_cvt_pk_bf16_f32 v81, v10, v11
	v_cvt_pk_bf16_f32 v80, v8, v9
	v_cvt_pk_bf16_f32 v79, v2, v3
	v_cvt_pk_bf16_f32 v78, v14, v15
	s_waitcnt lgkmcnt(0)
	v_mfma_f32_32x32x16_bf16 v[50:65], v[86:89], v[74:77], v[50:65]
	v_mfma_f32_32x32x16_bf16 v[34:49], v[86:89], v[78:81], v[34:49]
	ds_read_b128 v[86:89], v150 offset:56320
	ds_read_b128 v[18:21], v150 offset:44032
	ds_read_b128 v[22:25], v150 offset:45056
	ds_read_b128 v[26:29], v150 offset:46080
	ds_read_b128 v[30:33], v150 offset:47104
	ds_read_b128 v[100:103], v150 offset:57344
	s_waitcnt lgkmcnt(1)
	v_mfma_f32_32x32x16_bf16 v[18:33], v[86:89], v[4:7], v[18:33]
	ds_read_b128 v[2:5], v150 offset:48128
	ds_read_b128 v[6:9], v150 offset:49152
	ds_read_b128 v[10:13], v150 offset:50176
	ds_read_b128 v[14:17], v150 offset:51200
	s_waitcnt lgkmcnt(0)
	v_mfma_f32_32x32x16_bf16 v[2:17], v[86:89], v[92:95], v[2:17]
	v_mfma_f32_32x32x16_bf16 v[18:33], v[100:103], v[70:73], v[18:33]
	v_mfma_f32_32x32x16_bf16 v[2:17], v[100:103], v[66:69], v[2:17]
	ds_read_b128 v[66:69], v150 offset:58368
	ds_read_b128 v[70:73], v150 offset:59392
	s_waitcnt lgkmcnt(1)
	v_mfma_f32_32x32x16_bf16 v[18:33], v[66:69], v[82:85], v[18:33]
	v_mfma_f32_32x32x16_bf16 v[2:17], v[66:69], v[96:99], v[2:17]
	s_waitcnt lgkmcnt(0)
	v_mfma_f32_32x32x16_bf16 v[18:33], v[70:73], v[74:77], v[18:33]
	v_mfma_f32_32x32x16_bf16 v[2:17], v[70:73], v[78:81], v[2:17]
	s_nop 10
	v_mul_f32_e32 v66, v22, v22
	v_mul_f32_e32 v67, v23, v23
	v_mul_f32_e32 v68, v30, v30
	v_mul_f32_e32 v69, v31, v31
	v_mul_f32_e32 v70, v24, v24
	v_mul_f32_e32 v71, v25, v25
	v_pk_mul_f32 v[72:73], v[32:33], v[32:33]
	v_pk_mul_f32 v[74:75], v[20:21], v[20:21]
	v_pk_mul_f32 v[76:77], v[28:29], v[28:29]
	v_pk_mul_f32 v[78:79], v[26:27], v[26:27]
	v_pk_mul_f32 v[80:81], v[18:19], v[18:19]
	v_pk_fma_f32 v[78:79], v[58:59], v[58:59], v[78:79]
	v_pk_fma_f32 v[76:77], v[60:61], v[60:61], v[76:77]
	v_pk_fma_f32 v[74:75], v[52:53], v[52:53], v[74:75]
	v_pk_fma_f32 v[72:73], v[64:65], v[64:65], v[72:73]
	v_pk_fma_f32 v[70:71], v[56:57], v[56:57], v[70:71]
	v_pk_fma_f32 v[68:69], v[62:63], v[62:63], v[68:69]
	v_pk_fma_f32 v[66:67], v[54:55], v[54:55], v[66:67]
	v_pk_fma_f32 v[80:81], v[50:51], v[50:51], v[80:81]
	v_pk_add_f32 v[66:67], v[66:67], v[68:69]
	v_pk_add_f32 v[68:69], v[70:71], v[72:73]
	v_pk_add_f32 v[70:71], v[74:75], v[76:77]
	v_pk_add_f32 v[72:73], v[80:81], v[78:79]
	v_pk_add_f32 v[68:69], v[70:71], v[68:69]
	v_pk_add_f32 v[66:67], v[72:73], v[66:67]
	v_pk_mul_f32 v[72:73], v[14:15], v[14:15]
	v_pk_mov_b32 v[70:71], v[66:67], v[68:69] op_sel:[1,0]
	v_mov_b32_e32 v67, v69
	v_pk_add_f32 v[66:67], v[70:71], v[66:67]
	v_pk_mul_f32 v[70:71], v[6:7], v[6:7]
	v_pk_mul_f32 v[74:75], v[8:9], v[8:9]
	v_pk_mul_f32 v[76:77], v[16:17], v[16:17]
	v_pk_mul_f32 v[78:79], v[4:5], v[4:5]
	v_pk_mul_f32 v[80:81], v[12:13], v[12:13]
	v_pk_mul_f32 v[82:83], v[10:11], v[10:11]
	v_pk_mul_f32 v[84:85], v[2:3], v[2:3]
	v_pk_fma_f32 v[82:83], v[42:43], v[42:43], v[82:83]
	v_pk_fma_f32 v[80:81], v[44:45], v[44:45], v[80:81]
	v_pk_fma_f32 v[78:79], v[36:37], v[36:37], v[78:79]
	v_pk_fma_f32 v[76:77], v[48:49], v[48:49], v[76:77]
	v_pk_fma_f32 v[74:75], v[40:41], v[40:41], v[74:75]
	v_pk_fma_f32 v[72:73], v[46:47], v[46:47], v[72:73]
	v_pk_fma_f32 v[70:71], v[38:39], v[38:39], v[70:71]
	v_pk_fma_f32 v[84:85], v[34:35], v[34:35], v[84:85]
	v_pk_add_f32 v[70:71], v[70:71], v[72:73]
	v_pk_add_f32 v[72:73], v[74:75], v[76:77]
	v_pk_add_f32 v[74:75], v[78:79], v[80:81]
	v_pk_add_f32 v[76:77], v[84:85], v[82:83]
	v_pk_add_f32 v[72:73], v[74:75], v[72:73]
	v_pk_add_f32 v[70:71], v[76:77], v[70:71]
	v_pk_add_f32 v[66:67], v[66:67], v[66:67] op_sel:[0,1] op_sel_hi:[1,0]
	v_pk_mov_b32 v[74:75], v[70:71], v[72:73] op_sel:[1,0]
	v_mov_b32_e32 v71, v73
	v_pk_add_f32 v[70:71], v[74:75], v[70:71]
	v_mov_b32_e32 v69, v66
	v_pk_add_f32 v[70:71], v[70:71], v[70:71] op_sel:[0,1] op_sel_hi:[1,0]
	s_nop 0
	v_permlane32_swap_b32_e32 v66, v69
	v_mov_b32_e32 v68, v70
	s_nop 1
	v_permlane32_swap_b32_e32 v70, v68
	v_mov_b32_e32 v71, v66
	v_pk_add_f32 v[66:67], v[70:71], v[68:69]
	v_pk_fma_f32 v[66:67], v[66:67], s[0:1], v[152:153] op_sel_hi:[1,0,0]
	s_mov_b32 s1, 0x800000
	v_mul_f32_e32 v68, 0x4b800000, v67
	v_cmp_gt_f32_e32 vcc, s1, v67
	s_nop 1
	v_cndmask_b32_e32 v67, v67, v68, vcc
	v_rsq_f32_e32 v67, v67
	s_nop 0
	v_mul_f32_e32 v68, 0x45800000, v67
	v_cndmask_b32_e32 v68, v67, v68, vcc
	v_pk_mul_f32 v[158:159], v[50:51], v[68:69] op_sel_hi:[1,0]
	v_pk_mul_f32 v[50:51], v[18:19], v[68:69] op_sel_hi:[1,0]
	v_mul_f32_e32 v18, 0x4b800000, v66
	v_cmp_gt_f32_e32 vcc, s1, v66
	v_pk_mul_f32 v[80:81], v[60:61], v[68:69] op_sel_hi:[1,0]
	v_pk_mul_f32 v[60:61], v[28:29], v[68:69] op_sel_hi:[1,0]
	v_cndmask_b32_e32 v18, v66, v18, vcc
	v_rsq_f32_e32 v18, v18
	v_pk_mul_f32 v[78:79], v[58:59], v[68:69] op_sel_hi:[1,0]
	v_pk_mul_f32 v[160:161], v[52:53], v[68:69] op_sel_hi:[1,0]
	v_pk_mul_f32 v[82:83], v[54:55], v[68:69] op_sel_hi:[1,0]
	v_mul_f32_e32 v19, 0x45800000, v18
	v_cndmask_b32_e32 v28, v18, v19, vcc
	v_pk_mul_f32 v[168:169], v[56:57], v[68:69] op_sel_hi:[1,0]
	v_pk_mul_f32 v[58:59], v[26:27], v[68:69] op_sel_hi:[1,0]
	v_pk_mul_f32 v[52:53], v[20:21], v[68:69] op_sel_hi:[1,0]
	v_pk_mul_f32 v[54:55], v[22:23], v[68:69] op_sel_hi:[1,0]
	v_pk_mul_f32 v[56:57], v[24:25], v[68:69] op_sel_hi:[1,0]
	v_pk_mul_f32 v[18:19], v[42:43], v[28:29] op_sel_hi:[1,0]
	v_pk_mul_f32 v[20:21], v[44:45], v[28:29] op_sel_hi:[1,0]
	v_pk_mul_f32 v[22:23], v[46:47], v[28:29] op_sel_hi:[1,0]
	v_pk_mul_f32 v[26:27], v[48:49], v[28:29] op_sel_hi:[1,0]
	v_pk_mul_f32 v[162:163], v[34:35], v[28:29] op_sel_hi:[1,0]
	v_pk_mul_f32 v[164:165], v[36:37], v[28:29] op_sel_hi:[1,0]
	v_pk_mul_f32 v[166:167], v[38:39], v[28:29] op_sel_hi:[1,0]
	v_pk_mul_f32 v[24:25], v[40:41], v[28:29] op_sel_hi:[1,0]
	v_pk_mul_f32 v[104:105], v[2:3], v[28:29] op_sel_hi:[1,0]
	v_pk_mul_f32 v[112:113], v[4:5], v[28:29] op_sel_hi:[1,0]
	ds_read_b128 v[2:5], v150 offset:60416
	ds_read_b128 v[34:37], v174 offset:32768
	ds_read_b128 v[38:41], v174 offset:32800
	ds_read_b128 v[42:45], v174 offset:32832
	ds_read_b128 v[46:49], v174 offset:32864
	v_cvt_pk_bf16_f32 v129, v168, v169
	v_cvt_pk_bf16_f32 v128, v82, v83
	v_cvt_pk_bf16_f32 v127, v160, v161
	v_cvt_pk_bf16_f32 v126, v158, v159
	v_cvt_pk_bf16_f32 v137, v24, v25
	v_cvt_pk_bf16_f32 v136, v166, v167
	v_cvt_pk_bf16_f32 v135, v164, v165
	s_waitcnt lgkmcnt(0)
	v_mfma_f32_32x32x16_bf16 v[86:101], v[2:5], v[126:129], v[34:49]
	v_cvt_pk_bf16_f32 v134, v162, v163
	v_mul_f32_e32 v84, v62, v68
	v_mul_f32_e32 v85, v63, v68
	v_mul_f32_e32 v170, v64, v68
	v_mul_f32_e32 v171, v65, v68
	v_pk_mul_f32 v[62:63], v[30:31], v[68:69] op_sel_hi:[1,0]
	v_pk_mul_f32 v[64:65], v[32:33], v[68:69] op_sel_hi:[1,0]
	v_pk_mul_f32 v[116:117], v[6:7], v[28:29] op_sel_hi:[1,0]
	v_pk_mul_f32 v[154:155], v[8:9], v[28:29] op_sel_hi:[1,0]
	v_mfma_f32_32x32x16_bf16 v[34:49], v[2:5], v[134:137], v[34:49]
	ds_read_b128 v[6:9], v150 offset:61440
	ds_read_b128 v[66:69], v174 offset:32896
	ds_read_b128 v[106:109], v150 offset:64512
	v_cvt_pk_bf16_f32 v125, v170, v171
	v_cvt_pk_bf16_f32 v124, v84, v85
	v_cvt_pk_bf16_f32 v123, v80, v81
	v_cvt_pk_bf16_f32 v122, v78, v79
	v_cvt_pk_bf16_f32 v149, v26, v27
	v_cvt_pk_bf16_f32 v148, v22, v23
	v_cvt_pk_bf16_f32 v147, v20, v21
	v_cvt_pk_bf16_f32 v146, v18, v19
	s_waitcnt lgkmcnt(2)
	v_mfma_f32_32x32x16_bf16 v[86:101], v[6:9], v[122:125], v[86:101]
	v_mul_f32_e32 v102, v10, v28
	v_mul_f32_e32 v103, v11, v28
	v_mul_f32_e32 v110, v12, v28
	v_mul_f32_e32 v111, v13, v28
	v_mul_f32_e32 v114, v14, v28
	v_mul_f32_e32 v115, v15, v28
	v_pk_mul_f32 v[156:157], v[16:17], v[28:29] op_sel_hi:[1,0]
	ds_read_b128 v[176:179], v174 offset:33536
	ds_read_b128 v[180:183], v174 offset:33568
	ds_read_b128 v[184:187], v174 offset:33600
	ds_read_b128 v[28:31], v174 offset:33632
	ds_read_b128 v[188:191], v174 offset:33792
	ds_read_b128 v[192:195], v174 offset:33824
	ds_read_b128 v[196:199], v174 offset:33856
	ds_read_b128 v[200:203], v174 offset:33888
	ds_read_b128 v[204:207], v150 offset:62464
	v_cvt_pk_bf16_f32 v133, v56, v57
	v_mfma_f32_32x32x16_bf16 v[34:49], v[6:9], v[146:149], v[34:49]
	v_cvt_pk_bf16_f32 v132, v54, v55
	v_cvt_pk_bf16_f32 v131, v52, v53
	v_cvt_pk_bf16_f32 v130, v50, v51
	ds_read_b128 v[70:73], v174 offset:33664
	ds_read_b128 v[74:77], v174 offset:33920
	ds_read_b128 v[208:211], v150 offset:63488
	v_cvt_pk_bf16_f32 v145, v154, v155
	v_cvt_pk_bf16_f32 v144, v116, v117
	v_cvt_pk_bf16_f32 v143, v112, v113
	v_cvt_pk_bf16_f32 v142, v104, v105
	s_waitcnt lgkmcnt(3)
	v_mfma_f32_32x32x16_bf16 v[86:101], v[204:207], v[130:133], v[86:101]
	v_cvt_pk_bf16_f32 v121, v64, v65
	v_cvt_pk_bf16_f32 v120, v62, v63
	v_cvt_pk_bf16_f32 v119, v60, v61
	v_cvt_pk_bf16_f32 v118, v58, v59
	v_cvt_pk_bf16_f32 v141, v156, v157
	v_cvt_pk_bf16_f32 v140, v114, v115
	v_cvt_pk_bf16_f32 v139, v110, v111
	v_mfma_f32_32x32x16_bf16 v[34:49], v[204:207], v[142:145], v[34:49]
	v_cvt_pk_bf16_f32 v138, v102, v103
	v_fma_f32 v16, v30, v170, v202
	v_fma_f32 v17, v31, v171, v203
	v_fma_f32 v14, v28, v84, v200
	v_fma_f32 v15, v29, v85, v201
	v_pk_fma_f32 v[12:13], v[186:187], v[80:81], v[198:199]
	v_pk_fma_f32 v[10:11], v[184:185], v[78:79], v[196:197]
	v_pk_fma_f32 v[8:9], v[182:183], v[168:169], v[194:195]
	s_waitcnt lgkmcnt(0)
	v_mfma_f32_32x32x16_bf16 v[86:101], v[208:211], v[118:121], v[86:101]
	v_fma_f32 v6, v180, v82, v192
	v_fma_f32 v7, v181, v83, v193
	ds_read_b128 v[78:81], v174 offset:33760
	ds_read_b128 v[82:85], v174 offset:33248
	v_fma_f32 v4, v178, v160, v190
	v_fma_f32 v5, v179, v161, v191
	v_pk_fma_f32 v[2:3], v[176:177], v[158:159], v[188:189]
	v_pk_fma_f32 v[32:33], v[30:31], v[26:27], v[202:203]
	v_pk_fma_f32 v[30:31], v[28:29], v[22:23], v[200:201]
	v_pk_fma_f32 v[28:29], v[186:187], v[20:21], v[198:199]
	v_pk_fma_f32 v[26:27], v[184:185], v[18:19], v[196:197]
	v_pk_fma_f32 v[24:25], v[182:183], v[24:25], v[194:195]
	v_pk_fma_f32 v[22:23], v[180:181], v[166:167], v[192:193]
	v_pk_fma_f32 v[20:21], v[178:179], v[164:165], v[190:191]
	v_pk_fma_f32 v[18:19], v[176:177], v[162:163], v[188:189]
	ds_read_b128 v[158:161], v174 offset:33696
	ds_read_b128 v[162:165], v174 offset:33728
	ds_read_b128 v[166:169], v174 offset:33952
	ds_read_b128 v[176:179], v174 offset:33984
	ds_read_b128 v[180:183], v174 offset:34016
	ds_read_b128 v[184:187], v212 offset:11264
	v_mfma_f32_32x32x16_bf16 v[34:49], v[208:211], v[138:141], v[34:49]
	v_cvt_pk_bf16_f32 v86, v86, v87
	v_cvt_pk_bf16_f32 v87, v88, v89
	v_cvt_pk_bf16_f32 v88, v90, v91
	v_cvt_pk_bf16_f32 v89, v92, v93
	ds_read_b128 v[90:93], v212 offset:12288
	v_pk_max_i16 v86, v86, 0
	v_pk_max_i16 v87, v87, 0
	v_pk_max_i16 v88, v88, 0
	v_pk_max_i16 v89, v89, 0
	s_nop 1
	s_nop 0
	v_cvt_pk_bf16_f32 v188, v34, v35
	v_cvt_pk_bf16_f32 v189, v36, v37
	v_cvt_pk_bf16_f32 v190, v38, v39
	v_cvt_pk_bf16_f32 v191, v40, v41
	s_waitcnt lgkmcnt(1)
	v_mfma_f32_32x32x16_bf16 v[2:17], v[184:187], v[86:89], v[2:17]
	v_pk_max_i16 v188, v188, 0
	v_pk_max_i16 v189, v189, 0
	v_pk_max_i16 v190, v190, 0
	v_pk_max_i16 v191, v191, 0
	v_cvt_pk_bf16_f32 v94, v94, v95
	v_cvt_pk_bf16_f32 v95, v96, v97
	v_cvt_pk_bf16_f32 v96, v98, v99
	v_cvt_pk_bf16_f32 v97, v100, v101
	v_cvt_pk_bf16_f32 v98, v42, v43
	v_cvt_pk_bf16_f32 v99, v44, v45
	v_mfma_f32_32x32x16_bf16 v[18:33], v[184:187], v[188:191], v[18:33]
	ds_read_b128 v[184:187], v212 offset:19456
	v_cvt_pk_bf16_f32 v100, v46, v47
	v_cvt_pk_bf16_f32 v101, v48, v49
	v_fma_f32 v64, v80, v64, v182
	v_fma_f32 v65, v81, v65, v183
	v_pk_fma_f32 v[62:63], v[78:79], v[62:63], v[180:181]
	v_pk_fma_f32 v[60:61], v[164:165], v[60:61], v[178:179]
	v_pk_fma_f32 v[58:59], v[162:163], v[58:59], v[176:177]
	v_pk_max_i16 v94, v94, 0
	v_pk_max_i16 v95, v95, 0
	v_pk_max_i16 v96, v96, 0
	v_pk_max_i16 v97, v97, 0
	v_pk_max_i16 v98, v98, 0
	v_pk_max_i16 v99, v99, 0
	v_pk_max_i16 v100, v100, 0
	v_pk_max_i16 v101, v101, 0
	v_pk_fma_f32 v[56:57], v[160:161], v[56:57], v[168:169]
	s_waitcnt lgkmcnt(1)
	v_mfma_f32_32x32x16_bf16 v[2:17], v[90:93], v[94:97], v[2:17]
	v_fma_f32 v54, v158, v54, v166
	v_fma_f32 v55, v159, v55, v167
	v_fma_f32 v52, v72, v52, v76
	v_fma_f32 v53, v73, v53, v77
	v_fma_f32 v50, v70, v50, v74
	v_fma_f32 v51, v71, v51, v75
	v_pk_fma_f32 v[48:49], v[80:81], v[156:157], v[182:183]
	v_pk_fma_f32 v[46:47], v[78:79], v[114:115], v[180:181]
	v_pk_fma_f32 v[44:45], v[164:165], v[110:111], v[178:179]
	v_pk_fma_f32 v[42:43], v[162:163], v[102:103], v[176:177]
	v_mfma_f32_32x32x16_bf16 v[18:33], v[90:93], v[98:101], v[18:33]
	ds_read_b128 v[90:93], v212 offset:20480
	v_fma_f32 v40, v160, v154, v168
	v_fma_f32 v41, v161, v155, v169
	v_fma_f32 v38, v158, v116, v166
	v_fma_f32 v39, v159, v117, v167
	v_pk_fma_f32 v[36:37], v[72:73], v[112:113], v[76:77]
	v_pk_fma_f32 v[34:35], v[70:71], v[104:105], v[74:75]
	s_waitcnt lgkmcnt(1)
	v_mfma_f32_32x32x16_bf16 v[50:65], v[184:187], v[86:89], v[50:65]
	ds_read_b128 v[70:73], v174 offset:32928
	ds_read_b128 v[74:77], v174 offset:32960
	ds_read_b128 v[78:81], v174 offset:32992
	ds_read_b128 v[86:89], v174 offset:33024
	ds_read_b128 v[110:113], v212 offset:1024
	v_mfma_f32_32x32x16_bf16 v[34:49], v[184:187], v[188:191], v[34:49]
	s_waitcnt lgkmcnt(5)
	v_mfma_f32_32x32x16_bf16 v[50:65], v[90:93], v[94:97], v[50:65]
	v_mfma_f32_32x32x16_bf16 v[34:49], v[90:93], v[98:101], v[34:49]
	s_waitcnt lgkmcnt(2)
	v_mfma_f32_32x32x16_bf16 v[90:105], v[106:109], v[126:129], v[66:81]
	v_mfma_f32_32x32x16_bf16 v[66:81], v[106:109], v[134:137], v[66:81]
	ds_read_b128 v[106:109], v212 offset:0
	s_waitcnt lgkmcnt(0)
	v_mfma_f32_32x32x16_bf16 v[90:105], v[106:109], v[122:125], v[90:105]
	v_mfma_f32_32x32x16_bf16 v[66:81], v[106:109], v[146:149], v[66:81]
	ds_read_b128 v[106:109], v212 offset:2048
	v_mfma_f32_32x32x16_bf16 v[90:105], v[110:113], v[130:133], v[90:105]
	v_mfma_f32_32x32x16_bf16 v[66:81], v[110:113], v[142:145], v[66:81]
	ds_read_b128 v[110:113], v212 offset:13312
	s_waitcnt lgkmcnt(1)
	v_mfma_f32_32x32x16_bf16 v[90:105], v[106:109], v[118:121], v[90:105]
	v_mfma_f32_32x32x16_bf16 v[66:81], v[106:109], v[138:141], v[66:81]
	s_nop 10
	v_cvt_pk_bf16_f32 v90, v90, v91
	v_cvt_pk_bf16_f32 v91, v92, v93
	v_cvt_pk_bf16_f32 v92, v94, v95
	v_cvt_pk_bf16_f32 v94, v98, v99
	v_cvt_pk_bf16_f32 v95, v100, v101
	ds_read_b128 v[98:101], v212 offset:21504
	v_cvt_pk_bf16_f32 v66, v66, v67
	v_cvt_pk_bf16_f32 v67, v68, v69
	v_cvt_pk_bf16_f32 v68, v70, v71
	v_cvt_pk_bf16_f32 v93, v96, v97
	v_cvt_pk_bf16_f32 v69, v72, v73
	ds_read_b128 v[70:73], v212 offset:14336
	v_pk_max_i16 v90, v90, 0
	v_pk_max_i16 v91, v91, 0
	v_pk_max_i16 v92, v92, 0
	v_pk_max_i16 v93, v93, 0
	v_pk_max_i16 v66, v66, 0
	v_pk_max_i16 v67, v67, 0
	v_pk_max_i16 v68, v68, 0
	v_pk_max_i16 v69, v69, 0
	v_cvt_pk_bf16_f32 v96, v102, v103
	s_waitcnt lgkmcnt(2)
	v_mfma_f32_32x32x16_bf16 v[2:17], v[110:113], v[90:93], v[2:17]
	v_cvt_pk_bf16_f32 v97, v104, v105
	v_cvt_pk_bf16_f32 v74, v74, v75
	v_cvt_pk_bf16_f32 v75, v76, v77
	v_cvt_pk_bf16_f32 v76, v78, v79
	v_cvt_pk_bf16_f32 v77, v80, v81
	v_pk_max_i16 v94, v94, 0
	v_pk_max_i16 v95, v95, 0
	v_pk_max_i16 v96, v96, 0
	v_pk_max_i16 v97, v97, 0
	v_pk_max_i16 v74, v74, 0
	v_pk_max_i16 v75, v75, 0
	v_pk_max_i16 v76, v76, 0
	v_pk_max_i16 v77, v77, 0
	v_mfma_f32_32x32x16_bf16 v[18:33], v[110:113], v[66:69], v[18:33]
	s_waitcnt lgkmcnt(1)
	v_mfma_f32_32x32x16_bf16 v[34:49], v[98:101], v[66:69], v[34:49]
	ds_read_b128 v[66:69], v212 offset:22528
	v_mfma_f32_32x32x16_bf16 v[50:65], v[98:101], v[90:93], v[50:65]
	s_waitcnt lgkmcnt(1)
	v_mfma_f32_32x32x16_bf16 v[2:17], v[70:73], v[94:97], v[2:17]
	v_mfma_f32_32x32x16_bf16 v[18:33], v[70:73], v[74:77], v[18:33]
	ds_read_b128 v[78:81], v212 offset:3072
	s_waitcnt lgkmcnt(1)
	v_mfma_f32_32x32x16_bf16 v[50:65], v[66:69], v[94:97], v[50:65]
	ds_read_b128 v[90:93], v174 offset:33056
	ds_read_b128 v[94:97], v174 offset:33088
	ds_read_b128 v[98:101], v174 offset:33120
	ds_read_b128 v[70:73], v174 offset:33152
	v_mfma_f32_32x32x16_bf16 v[34:49], v[66:69], v[74:77], v[34:49]
	ds_read_b128 v[66:69], v212 offset:4096
	ds_read_b128 v[74:77], v212 offset:5120
	s_waitcnt lgkmcnt(3)
	v_mfma_f32_32x32x16_bf16 v[102:117], v[78:81], v[126:129], v[86:101]
	v_mfma_f32_32x32x16_bf16 v[86:101], v[78:81], v[134:137], v[86:101]
	s_waitcnt lgkmcnt(1)
	v_mfma_f32_32x32x16_bf16 v[86:101], v[66:69], v[146:149], v[86:101]
	v_mfma_f32_32x32x16_bf16 v[102:117], v[66:69], v[122:125], v[102:117]
	ds_read_b128 v[66:69], v212 offset:6144
	s_waitcnt lgkmcnt(1)
	v_mfma_f32_32x32x16_bf16 v[86:101], v[74:77], v[142:145], v[86:101]
	v_mfma_f32_32x32x16_bf16 v[102:117], v[74:77], v[130:133], v[102:117]
	ds_read_b128 v[74:77], v212 offset:15360
	s_waitcnt lgkmcnt(1)
	v_mfma_f32_32x32x16_bf16 v[86:101], v[66:69], v[138:141], v[86:101]
	v_mfma_f32_32x32x16_bf16 v[102:117], v[66:69], v[118:121], v[102:117]
	s_nop 10
	v_cvt_pk_bf16_f32 v78, v86, v87
	v_cvt_pk_bf16_f32 v80, v90, v91
	v_cvt_pk_bf16_f32 v79, v88, v89
	v_cvt_pk_bf16_f32 v81, v92, v93
	ds_read_b128 v[86:89], v212 offset:16384
	ds_read_b128 v[90:93], v212 offset:23552
	v_cvt_pk_bf16_f32 v66, v102, v103
	v_cvt_pk_bf16_f32 v67, v104, v105
	v_cvt_pk_bf16_f32 v68, v106, v107
	v_cvt_pk_bf16_f32 v69, v108, v109
	v_pk_max_i16 v66, v66, 0
	v_pk_max_i16 v67, v67, 0
	v_pk_max_i16 v68, v68, 0
	v_pk_max_i16 v69, v69, 0
	v_pk_max_i16 v78, v78, 0
	v_pk_max_i16 v79, v79, 0
	v_pk_max_i16 v80, v80, 0
	v_pk_max_i16 v81, v81, 0
	v_cvt_pk_bf16_f32 v94, v94, v95
	s_waitcnt lgkmcnt(2)
	v_mfma_f32_32x32x16_bf16 v[18:33], v[74:77], v[78:81], v[18:33]
	v_cvt_pk_bf16_f32 v95, v96, v97
	v_cvt_pk_bf16_f32 v96, v98, v99
	v_cvt_pk_bf16_f32 v97, v100, v101
	v_pk_max_i16 v94, v94, 0
	v_pk_max_i16 v95, v95, 0
	v_pk_max_i16 v96, v96, 0
	v_pk_max_i16 v97, v97, 0
	v_mfma_f32_32x32x16_bf16 v[2:17], v[74:77], v[66:69], v[2:17]
	v_cvt_pk_bf16_f32 v74, v110, v111
	v_cvt_pk_bf16_f32 v75, v112, v113
	v_cvt_pk_bf16_f32 v76, v114, v115
	v_cvt_pk_bf16_f32 v77, v116, v117
	v_pk_max_i16 v74, v74, 0
	v_pk_max_i16 v75, v75, 0
	v_pk_max_i16 v76, v76, 0
	v_pk_max_i16 v77, v77, 0
	s_waitcnt lgkmcnt(0)
	v_mfma_f32_32x32x16_bf16 v[50:65], v[90:93], v[66:69], v[50:65]
	ds_read_b128 v[66:69], v212 offset:24576
	v_mfma_f32_32x32x16_bf16 v[34:49], v[90:93], v[78:81], v[34:49]
	ds_read_b128 v[102:105], v212 offset:7168
	v_mfma_f32_32x32x16_bf16 v[2:17], v[86:89], v[74:77], v[2:17]
	s_waitcnt lgkmcnt(1)
	v_mfma_f32_32x32x16_bf16 v[50:65], v[66:69], v[74:77], v[50:65]
	ds_read_b128 v[74:77], v174 offset:33184
	ds_read_b128 v[78:81], v174 offset:33216
	v_mfma_f32_32x32x16_bf16 v[34:49], v[66:69], v[94:97], v[34:49]
	ds_read_b128 v[66:69], v212 offset:8192
	v_mfma_f32_32x32x16_bf16 v[18:33], v[86:89], v[94:97], v[18:33]
	s_waitcnt lgkmcnt(1)
	v_mfma_f32_32x32x16_bf16 v[86:101], v[102:105], v[126:129], v[70:85]
	v_mfma_f32_32x32x16_bf16 v[70:85], v[102:105], v[134:137], v[70:85]
	ds_read_b128 v[102:105], v212 offset:9216
	v_lshlrev_b32_e32 v135, 2, v1
	v_add_u32_e32 v134, v172, v174
	s_waitcnt lgkmcnt(1)
	v_mfma_f32_32x32x16_bf16 v[86:101], v[66:69], v[122:125], v[86:101]
	v_mfma_f32_32x32x16_bf16 v[70:85], v[66:69], v[146:149], v[70:85]
	ds_read_b128 v[66:69], v212 offset:10240
	s_waitcnt lgkmcnt(1)
	v_mfma_f32_32x32x16_bf16 v[86:101], v[102:105], v[130:133], v[86:101]
	v_mfma_f32_32x32x16_bf16 v[70:85], v[102:105], v[142:145], v[70:85]
	ds_read_b128 v[102:105], v212 offset:17408
	s_waitcnt lgkmcnt(1)
	v_mfma_f32_32x32x16_bf16 v[86:101], v[66:69], v[118:121], v[86:101]
	v_mfma_f32_32x32x16_bf16 v[70:85], v[66:69], v[138:141], v[70:85]
	s_nop 10
	v_cvt_pk_bf16_f32 v68, v90, v91
	v_cvt_pk_bf16_f32 v69, v92, v93
	ds_read_b128 v[90:93], v212 offset:25600
	v_cvt_pk_bf16_f32 v66, v86, v87
	v_cvt_pk_bf16_f32 v67, v88, v89
	v_pk_max_i16 v66, v66, 0
	v_pk_max_i16 v67, v67, 0
	v_pk_max_i16 v68, v68, 0
	v_pk_max_i16 v69, v69, 0
	v_cvt_pk_bf16_f32 v70, v70, v71
	v_cvt_pk_bf16_f32 v71, v72, v73
	s_waitcnt lgkmcnt(1)
	v_mfma_f32_32x32x16_bf16 v[2:17], v[102:105], v[66:69], v[2:17]
	v_cvt_pk_bf16_f32 v72, v74, v75
	v_cvt_pk_bf16_f32 v73, v76, v77
	ds_read_b128 v[74:77], v212 offset:18432
	v_cvt_pk_bf16_f32 v86, v94, v95
	v_cvt_pk_bf16_f32 v87, v96, v97
	v_cvt_pk_bf16_f32 v88, v98, v99
	s_waitcnt lgkmcnt(1)
	v_mfma_f32_32x32x16_bf16 v[50:65], v[90:93], v[66:69], v[50:65]
	ds_read_b128 v[66:69], v212 offset:26624
	v_cvt_pk_bf16_f32 v89, v100, v101
	v_pk_max_i16 v86, v86, 0
	v_pk_max_i16 v87, v87, 0
	v_pk_max_i16 v88, v88, 0
	v_pk_max_i16 v89, v89, 0
	v_pk_max_i16 v70, v70, 0
	v_pk_max_i16 v71, v71, 0
	v_pk_max_i16 v72, v72, 0
	v_pk_max_i16 v73, v73, 0
	v_cvt_pk_bf16_f32 v78, v78, v79
	v_cvt_pk_bf16_f32 v79, v80, v81
	s_waitcnt lgkmcnt(1)
	v_mfma_f32_32x32x16_bf16 v[2:17], v[74:77], v[86:89], v[2:17]
	v_cvt_pk_bf16_f32 v80, v82, v83
	v_cvt_pk_bf16_f32 v81, v84, v85
	v_pk_max_i16 v78, v78, 0
	v_pk_max_i16 v79, v79, 0
	v_pk_max_i16 v80, v80, 0
	v_pk_max_i16 v81, v81, 0
	s_waitcnt lgkmcnt(0)
	v_mfma_f32_32x32x16_bf16 v[50:65], v[66:69], v[86:89], v[50:65]
	v_mfma_f32_32x32x16_bf16 v[34:49], v[90:93], v[70:73], v[34:49]
	s_nop 10
	v_add_f32_e32 v130, v10, v58
	v_add_f32_e32 v131, v11, v59
	v_add_f32_e32 v132, v12, v60
	v_add_f32_e32 v133, v13, v61
	v_add_f32_e32 v138, v4, v52
	v_add_f32_e32 v139, v5, v53
	v_pk_add_f32 v[140:141], v[16:17], v[64:65]
	v_pk_add_f32 v[142:143], v[8:9], v[56:57]
	v_pk_add_f32 v[144:145], v[14:15], v[62:63]
	v_pk_add_f32 v[146:147], v[6:7], v[54:55]
	v_mfma_f32_32x32x16_bf16 v[18:33], v[102:105], v[70:73], v[18:33]
	ds_read2st64_b32 v[70:71], v135 offset0:133 offset1:134
	v_add_f32_e32 v148, v2, v50
	v_add_f32_e32 v149, v3, v51
	v_add_f32_e32 v144, v146, v144
	v_add_f32_e32 v145, v147, v145
	v_pk_add_f32 v[140:141], v[142:143], v[140:141]
	v_pk_add_f32 v[132:133], v[138:139], v[132:133]
	v_pk_add_f32 v[130:131], v[148:149], v[130:131]
	v_pk_add_f32 v[132:133], v[132:133], v[140:141]
	v_pk_add_f32 v[130:131], v[130:131], v[144:145]
	v_mfma_f32_32x32x16_bf16 v[34:49], v[66:69], v[78:81], v[34:49]
	v_pk_mov_b32 v[138:139], v[130:131], v[132:133] op_sel:[1,0]
	v_mov_b32_e32 v131, v133
	s_waitcnt vmcnt(0) lgkmcnt(0)
	v_mul_f32_e32 v66, v175, v70
	v_pk_add_f32 v[130:131], v[138:139], v[130:131]
	ds_write_b32 v173, v66 offset:512
	v_mul_f32_e32 v66, v175, v71
	v_pk_add_f32 v[130:131], v[130:131], v[130:131] op_sel:[0,1] op_sel_hi:[1,0]
	s_waitcnt lgkmcnt(0)
	ds_read_b128 v[102:105], v174 offset:34560
	ds_read_b128 v[98:101], v174 offset:34592
	ds_read_b128 v[110:113], v174 offset:34624
	ds_read_b128 v[106:109], v174 offset:34656
	ds_read_b128 v[114:117], v174 offset:34688
	ds_read_b128 v[122:125], v174 offset:34720
	ds_read_b128 v[118:121], v174 offset:34752
	ds_read_b128 v[126:129], v174 offset:34784
	v_mov_b32_dpp v66, v66 quad_perm:[1,0,3,2] row_mask:0xf bank_mask:0xf bound_ctrl:1
	v_mov_b32_e32 v131, v130
	v_fmac_f32_e32 v66, v175, v71
	s_nop 0
	v_permlane32_swap_b32_e32 v130, v131
	v_add_f32_dpp v66, v66, v66 quad_perm:[2,3,0,1] row_mask:0xf bank_mask:0xf bound_ctrl:1
	v_add_f32_e32 v130, v130, v131
	v_fmamk_f32 v65, v130, 0xbc800000, v65
	v_add_f32_dpp v66, v66, v66 row_half_mirror row_mask:0xf bank_mask:0xf bound_ctrl:1
	v_fmamk_f32 v64, v130, 0xbc800000, v64
	v_fmamk_f32 v63, v130, 0xbc800000, v63
	v_fmamk_f32 v62, v130, 0xbc800000, v62
	v_fmamk_f32 v61, v130, 0xbc800000, v61
	v_fmamk_f32 v60, v130, 0xbc800000, v60
	v_fmamk_f32 v59, v130, 0xbc800000, v59
	v_fmamk_f32 v58, v130, 0xbc800000, v58
	v_fmamk_f32 v57, v130, 0xbc800000, v57
	v_fmamk_f32 v56, v130, 0xbc800000, v56
	v_fmamk_f32 v55, v130, 0xbc800000, v55
	v_fmamk_f32 v54, v130, 0xbc800000, v54
	v_fmamk_f32 v53, v130, 0xbc800000, v53
	v_fmamk_f32 v52, v130, 0xbc800000, v52
	v_fmamk_f32 v51, v130, 0xbc800000, v51
	v_fmac_f32_e32 v50, 0xbc800000, v130
	v_add_f32_dpp v66, v66, v66 row_ror:8 row_mask:0xf bank_mask:0xf bound_ctrl:1
	v_fmamk_f32 v17, v130, 0xbc800000, v17
	v_fmamk_f32 v16, v130, 0xbc800000, v16
	v_fmamk_f32 v15, v130, 0xbc800000, v15
	v_fmamk_f32 v14, v130, 0xbc800000, v14
	v_fmamk_f32 v13, v130, 0xbc800000, v13
	v_fmamk_f32 v12, v130, 0xbc800000, v12
	v_fmamk_f32 v11, v130, 0xbc800000, v11
	v_fmamk_f32 v10, v130, 0xbc800000, v10
	v_fmamk_f32 v9, v130, 0xbc800000, v9
	v_fmamk_f32 v8, v130, 0xbc800000, v8
	v_fmamk_f32 v7, v130, 0xbc800000, v7
	v_fmamk_f32 v6, v130, 0xbc800000, v6
	v_fmamk_f32 v5, v130, 0xbc800000, v5
	v_fmamk_f32 v4, v130, 0xbc800000, v4
	v_fmamk_f32 v3, v130, 0xbc800000, v3
	v_fmac_f32_e32 v2, 0xbc800000, v130
	v_pk_mul_f32 v[130:131], v[54:55], v[54:55]
	v_pk_mul_f32 v[132:133], v[62:63], v[62:63]
	v_pk_mul_f32 v[138:139], v[50:51], v[50:51]
	v_pk_mul_f32 v[140:141], v[58:59], v[58:59]
	v_pk_mul_f32 v[142:143], v[56:57], v[56:57]
	v_pk_mul_f32 v[144:145], v[64:65], v[64:65]
	v_pk_mul_f32 v[146:147], v[52:53], v[52:53]
	v_pk_mul_f32 v[148:149], v[60:61], v[60:61]
	v_mov_b32_e32 v67, v66
	v_pk_fma_f32 v[148:149], v[12:13], v[12:13], v[148:149]
	v_pk_fma_f32 v[146:147], v[4:5], v[4:5], v[146:147]
	v_pk_fma_f32 v[144:145], v[16:17], v[16:17], v[144:145]
	v_pk_fma_f32 v[142:143], v[8:9], v[8:9], v[142:143]
	v_pk_fma_f32 v[140:141], v[10:11], v[10:11], v[140:141]
	v_pk_fma_f32 v[138:139], v[2:3], v[2:3], v[138:139]
	v_pk_fma_f32 v[132:133], v[14:15], v[14:15], v[132:133]
	v_pk_fma_f32 v[130:131], v[6:7], v[6:7], v[130:131]
	v_permlane16_swap_b32_e32 v66, v67
	v_pk_add_f32 v[130:131], v[130:131], v[132:133]
	v_pk_add_f32 v[132:133], v[138:139], v[140:141]
	v_pk_add_f32 v[138:139], v[142:143], v[144:145]
	v_pk_add_f32 v[140:141], v[146:147], v[148:149]
	v_mfma_f32_32x32x16_bf16 v[18:33], v[74:77], v[78:81], v[18:33]
	v_add_f32_e32 v136, v66, v67
	ds_read_b128 v[70:73], v134 offset:512
	ds_read_b128 v[66:69], v134 offset:544
	ds_read_b128 v[78:81], v134 offset:576
	ds_read_b128 v[74:77], v134 offset:608
	ds_read_b128 v[82:85], v134 offset:640
	ds_read_b128 v[90:93], v134 offset:672
	ds_read_b128 v[86:89], v134 offset:704
	ds_read_b128 v[94:97], v134 offset:736
	v_pk_add_f32 v[138:139], v[140:141], v[138:139]
	v_pk_add_f32 v[130:131], v[132:133], v[130:131]
	s_waitcnt lgkmcnt(8)
	v_pk_mul_f32 v[140:141], v[126:127], v[62:63]
	v_pk_mov_b32 v[132:133], v[130:131], v[138:139] op_sel:[1,0]
	v_mov_b32_e32 v131, v139
	v_pk_mul_f32 v[138:139], v[122:123], v[54:55]
	v_pk_mul_f32 v[142:143], v[114:115], v[50:51]
	v_pk_mul_f32 v[144:145], v[118:119], v[58:59]
	v_pk_mul_f32 v[146:147], v[124:125], v[56:57]
	v_pk_mul_f32 v[148:149], v[128:129], v[64:65]
	v_pk_mul_f32 v[154:155], v[116:117], v[52:53]
	v_pk_mul_f32 v[156:157], v[120:121], v[60:61]
	v_pk_fma_f32 v[154:155], v[104:105], v[4:5], v[154:155]
	v_pk_fma_f32 v[156:157], v[112:113], v[12:13], v[156:157]
	v_pk_fma_f32 v[148:149], v[108:109], v[16:17], v[148:149]
	v_pk_fma_f32 v[146:147], v[100:101], v[8:9], v[146:147]
	v_pk_fma_f32 v[144:145], v[110:111], v[10:11], v[144:145]
	v_pk_fma_f32 v[142:143], v[102:103], v[2:3], v[142:143]
	v_pk_fma_f32 v[140:141], v[106:107], v[14:15], v[140:141]
	v_pk_fma_f32 v[138:139], v[98:99], v[6:7], v[138:139]
	v_pk_add_f32 v[130:131], v[132:133], v[130:131]
	v_pk_add_f32 v[138:139], v[138:139], v[140:141]
	v_pk_add_f32 v[140:141], v[142:143], v[144:145]
	v_pk_add_f32 v[142:143], v[146:147], v[148:149]
	v_pk_add_f32 v[144:145], v[154:155], v[156:157]
	v_pk_add_f32 v[132:133], v[130:131], v[130:131] op_sel:[0,1] op_sel_hi:[1,0]
	v_pk_add_f32 v[142:143], v[144:145], v[142:143]
	v_pk_add_f32 v[138:139], v[140:141], v[138:139]
	v_add_f32_e32 v133, v142, v143
	v_add_f32_e32 v130, v138, v139
	s_waitcnt lgkmcnt(2)
	v_pk_mul_f32 v[138:139], v[90:91], v[54:55]
	s_waitcnt lgkmcnt(0)
	v_pk_mul_f32 v[140:141], v[94:95], v[62:63]
	v_pk_mul_f32 v[142:143], v[82:83], v[50:51]
	v_pk_mul_f32 v[144:145], v[86:87], v[58:59]
	v_pk_mul_f32 v[146:147], v[92:93], v[56:57]
	v_pk_mul_f32 v[148:149], v[96:97], v[64:65]
	v_pk_mul_f32 v[154:155], v[84:85], v[52:53]
	v_pk_mul_f32 v[156:157], v[88:89], v[60:61]
	v_add_f32_e32 v130, v130, v133
	v_pk_fma_f32 v[156:157], v[80:81], v[12:13], v[156:157]
	v_pk_fma_f32 v[154:155], v[72:73], v[4:5], v[154:155]
	v_pk_fma_f32 v[148:149], v[76:77], v[16:17], v[148:149]
	v_pk_fma_f32 v[146:147], v[68:69], v[8:9], v[146:147]
	v_pk_fma_f32 v[144:145], v[78:79], v[10:11], v[144:145]
	v_pk_fma_f32 v[142:143], v[70:71], v[2:3], v[142:143]
	v_pk_fma_f32 v[140:141], v[74:75], v[14:15], v[140:141]
	v_pk_fma_f32 v[138:139], v[66:67], v[6:7], v[138:139]
	v_mov_b32_e32 v133, v130
	v_pk_add_f32 v[138:139], v[138:139], v[140:141]
	v_pk_add_f32 v[140:141], v[142:143], v[144:145]
	v_pk_add_f32 v[142:143], v[146:147], v[148:149]
	v_pk_add_f32 v[144:145], v[154:155], v[156:157]
	v_permlane32_swap_b32_e32 v130, v133
	v_pk_add_f32 v[142:143], v[144:145], v[142:143]
	v_add_f32_e32 v160, v130, v133
	v_pk_add_f32 v[138:139], v[140:141], v[138:139]
	v_add_f32_e32 v133, v142, v143
	v_pk_add_f32 v[140:141], v[26:27], v[42:43]
	v_pk_add_f32 v[142:143], v[28:29], v[44:45]
	v_pk_add_f32 v[144:145], v[20:21], v[36:37]
	v_pk_add_f32 v[146:147], v[32:33], v[48:49]
	v_pk_add_f32 v[148:149], v[24:25], v[40:41]
	v_pk_add_f32 v[154:155], v[30:31], v[46:47]
	v_pk_add_f32 v[156:157], v[22:23], v[38:39]
	v_pk_add_f32 v[158:159], v[18:19], v[34:35]
	v_pk_add_f32 v[154:155], v[156:157], v[154:155]
	v_pk_add_f32 v[146:147], v[148:149], v[146:147]
	v_pk_add_f32 v[142:143], v[144:145], v[142:143]
	v_pk_add_f32 v[140:141], v[158:159], v[140:141]
	v_pk_add_f32 v[142:143], v[142:143], v[146:147]
	v_pk_add_f32 v[140:141], v[140:141], v[154:155]
	v_add_f32_e32 v130, v138, v139
	v_pk_mov_b32 v[144:145], v[140:141], v[142:143] op_sel:[1,0]
	v_mov_b32_e32 v141, v143
	v_pk_add_f32 v[140:141], v[144:145], v[140:141]
	v_add_f32_e32 v133, v130, v133
	v_pk_add_f32 v[140:141], v[140:141], v[140:141] op_sel:[0,1] op_sel_hi:[1,0]
	v_mov_b32_e32 v131, v132
	v_mov_b32_e32 v130, v140
	s_nop 1
	v_permlane32_swap_b32_e32 v140, v130
	v_add_f32_e32 v130, v140, v130
	v_fmamk_f32 v49, v130, 0xbc800000, v49
	v_fmamk_f32 v48, v130, 0xbc800000, v48
	v_fmamk_f32 v47, v130, 0xbc800000, v47
	v_fmamk_f32 v46, v130, 0xbc800000, v46
	v_fmamk_f32 v45, v130, 0xbc800000, v45
	v_fmamk_f32 v44, v130, 0xbc800000, v44
	v_fmamk_f32 v43, v130, 0xbc800000, v43
	v_fmamk_f32 v42, v130, 0xbc800000, v42
	v_fmamk_f32 v41, v130, 0xbc800000, v41
	v_fmamk_f32 v40, v130, 0xbc800000, v40
	v_fmamk_f32 v39, v130, 0xbc800000, v39
	v_fmamk_f32 v38, v130, 0xbc800000, v38
	v_fmamk_f32 v37, v130, 0xbc800000, v37
	v_fmamk_f32 v36, v130, 0xbc800000, v36
	v_fmamk_f32 v35, v130, 0xbc800000, v35
	v_fmac_f32_e32 v34, 0xbc800000, v130
	v_fmamk_f32 v33, v130, 0xbc800000, v33
	v_fmamk_f32 v32, v130, 0xbc800000, v32
	v_fmamk_f32 v31, v130, 0xbc800000, v31
	v_fmamk_f32 v30, v130, 0xbc800000, v30
	v_fmamk_f32 v29, v130, 0xbc800000, v29
	v_fmamk_f32 v28, v130, 0xbc800000, v28
	v_fmamk_f32 v27, v130, 0xbc800000, v27
	v_fmamk_f32 v26, v130, 0xbc800000, v26
	v_fmamk_f32 v25, v130, 0xbc800000, v25
	v_fmamk_f32 v24, v130, 0xbc800000, v24
	v_fmamk_f32 v23, v130, 0xbc800000, v23
	v_fmamk_f32 v22, v130, 0xbc800000, v22
	v_fmamk_f32 v21, v130, 0xbc800000, v21
	v_fmamk_f32 v20, v130, 0xbc800000, v20
	v_fmamk_f32 v19, v130, 0xbc800000, v19
	v_fmac_f32_e32 v18, 0xbc800000, v130
	v_pk_mul_f32 v[140:141], v[38:39], v[38:39]
	v_pk_mul_f32 v[142:143], v[46:47], v[46:47]
	v_pk_mul_f32 v[144:145], v[34:35], v[34:35]
	v_pk_mul_f32 v[146:147], v[42:43], v[42:43]
	v_pk_mul_f32 v[148:149], v[40:41], v[40:41]
	v_pk_mul_f32 v[154:155], v[48:49], v[48:49]
	v_pk_mul_f32 v[156:157], v[36:37], v[36:37]
	v_pk_mul_f32 v[158:159], v[44:45], v[44:45]
	v_pk_fma_f32 v[156:157], v[20:21], v[20:21], v[156:157]
	v_pk_fma_f32 v[158:159], v[28:29], v[28:29], v[158:159]
	v_pk_fma_f32 v[154:155], v[32:33], v[32:33], v[154:155]
	v_pk_fma_f32 v[148:149], v[24:25], v[24:25], v[148:149]
	v_pk_fma_f32 v[146:147], v[26:27], v[26:27], v[146:147]
	v_pk_fma_f32 v[144:145], v[18:19], v[18:19], v[144:145]
	v_pk_fma_f32 v[142:143], v[30:31], v[30:31], v[142:143]
	v_pk_fma_f32 v[140:141], v[22:23], v[22:23], v[140:141]
	v_permlane32_swap_b32_e32 v132, v131
	v_pk_add_f32 v[140:141], v[140:141], v[142:143]
	v_pk_add_f32 v[142:143], v[144:145], v[146:147]
	v_pk_add_f32 v[144:145], v[148:149], v[154:155]
	v_pk_add_f32 v[146:147], v[156:157], v[158:159]
	v_pk_add_f32 v[140:141], v[142:143], v[140:141]
	v_pk_add_f32 v[144:145], v[146:147], v[144:145]
	v_pk_mul_f32 v[122:123], v[122:123], v[38:39]
	v_pk_mov_b32 v[142:143], v[140:141], v[144:145] op_sel:[1,0]
	v_mov_b32_e32 v141, v145
	v_pk_add_f32 v[140:141], v[142:143], v[140:141]
	v_pk_mul_f32 v[126:127], v[126:127], v[46:47]
	v_pk_add_f32 v[140:141], v[140:141], v[140:141] op_sel:[0,1] op_sel_hi:[1,0]
	v_pk_mul_f32 v[114:115], v[114:115], v[34:35]
	v_mov_b32_e32 v130, v140
	s_nop 1
	v_permlane32_swap_b32_e32 v140, v130
	v_mov_b32_e32 v141, v132
	v_pk_add_f32 v[130:131], v[140:141], v[130:131]
	v_pk_mul_f32 v[118:119], v[118:119], v[42:43]
	v_pk_fma_f32 v[130:131], v[130:131], s[0:1], v[152:153] op_sel_hi:[1,0,0]
	v_pk_mul_f32 v[124:125], v[124:125], v[40:41]
	v_mul_f32_e32 v132, 0x4b800000, v131
	v_cmp_gt_f32_e32 vcc, s1, v131
	v_pk_mul_f32 v[128:129], v[128:129], v[48:49]
	v_pk_mul_f32 v[116:117], v[116:117], v[36:37]
	v_pk_mul_f32 v[120:121], v[120:121], v[44:45]
	v_cndmask_b32_e32 v131, v131, v132, vcc
	v_mul_f32_e32 v132, 0x4b800000, v130
	v_cmp_gt_f32_e64 s[0:1], s1, v130
	v_pk_fma_f32 v[112:113], v[112:113], v[28:29], v[120:121]
	v_pk_fma_f32 v[104:105], v[104:105], v[20:21], v[116:117]
	v_pk_fma_f32 v[108:109], v[108:109], v[32:33], v[128:129]
	v_pk_fma_f32 v[100:101], v[100:101], v[24:25], v[124:125]
	v_pk_fma_f32 v[110:111], v[110:111], v[26:27], v[118:119]
	v_pk_fma_f32 v[102:103], v[102:103], v[18:19], v[114:115]
	v_pk_fma_f32 v[106:107], v[106:107], v[30:31], v[126:127]
	v_pk_fma_f32 v[98:99], v[98:99], v[22:23], v[122:123]
	v_rsq_f32_e32 v131, v131
	v_cndmask_b32_e64 v130, v130, v132, s[0:1]
	v_pk_add_f32 v[98:99], v[98:99], v[106:107]
	v_pk_add_f32 v[102:103], v[102:103], v[110:111]
	v_pk_add_f32 v[100:101], v[100:101], v[108:109]
	v_pk_add_f32 v[104:105], v[104:105], v[112:113]
	v_rsq_f32_e32 v132, v130
	v_pk_add_f32 v[100:101], v[104:105], v[100:101]
	v_pk_add_f32 v[98:99], v[102:103], v[98:99]
	v_mul_f32_e32 v130, 0x45800000, v131
	v_add_f32_e32 v98, v98, v99
	v_add_f32_e32 v99, v100, v101
	v_add_f32_e32 v98, v98, v99
	v_mov_b32_e32 v99, v98
	v_pk_mul_f32 v[90:91], v[90:91], v[38:39]
	v_pk_mul_f32 v[94:95], v[94:95], v[46:47]
	v_pk_mul_f32 v[82:83], v[82:83], v[34:35]
	v_pk_mul_f32 v[86:87], v[86:87], v[42:43]
	v_cndmask_b32_e32 v130, v131, v130, vcc
	v_mul_f32_e32 v131, 0x45800000, v132
	v_permlane32_swap_b32_e32 v98, v99
	v_pk_fma_f32 v[78:79], v[78:79], v[26:27], v[86:87]
	v_pk_fma_f32 v[70:71], v[70:71], v[18:19], v[82:83]
	v_pk_fma_f32 v[74:75], v[74:75], v[30:31], v[94:95]
	v_pk_fma_f32 v[66:67], v[66:67], v[22:23], v[90:91]
	v_cndmask_b32_e64 v131, v132, v131, s[0:1]
	v_add_f32_e32 v98, v98, v99
	v_pk_add_f32 v[66:67], v[66:67], v[74:75]
	v_pk_add_f32 v[70:71], v[70:71], v[78:79]
	v_mul_f32_e32 v139, v160, v130
	v_mul_f32_e32 v98, v98, v131
	v_pk_add_f32 v[66:67], v[70:71], v[66:67]
	v_cmp_gt_u32_e32 vcc, 32, v1
	v_add_f32_e32 v66, v66, v67
	v_pk_mul_f32 v[92:93], v[92:93], v[40:41]
	v_cndmask_b32_e32 v67, v98, v139, vcc
	v_add_f32_e32 v67, s12, v67
	v_pk_mul_f32 v[96:97], v[96:97], v[48:49]
	v_pk_mul_f32 v[84:85], v[84:85], v[36:37]
	v_pk_mul_f32 v[88:89], v[88:89], v[44:45]
	v_mul_f32_e32 v67, 0xbfb8aa3b, v67
	v_pk_fma_f32 v[80:81], v[80:81], v[28:29], v[88:89]
	v_pk_fma_f32 v[72:73], v[72:73], v[20:21], v[84:85]
	v_pk_fma_f32 v[76:77], v[76:77], v[32:33], v[96:97]
	v_pk_fma_f32 v[68:69], v[68:69], v[24:25], v[92:93]
	v_exp_f32_e32 v70, v67
	v_pk_add_f32 v[68:69], v[68:69], v[76:77]
	v_pk_add_f32 v[72:73], v[72:73], v[80:81]
	v_cmp_lt_i32_e64 s[0:1], 0, v151
	v_pk_add_f32 v[68:69], v[72:73], v[68:69]
	v_mov_b32_e32 v137, v136
	v_add_f32_e32 v67, v68, v69
	v_add_f32_e32 v67, v66, v67
	v_add_f32_e32 v66, 1.0, v70
	v_rcp_f32_e32 v66, v66
	v_mov_b32_e32 v69, 0xff800000
	v_mov_b32_e32 v138, v133
	v_mov_b32_e32 v68, v67
	v_cndmask_b32_e64 v70, v69, v66, s[0:1]
	v_mbcnt_lo_u32_b32 v66, -1, 0
	v_mbcnt_hi_u32_b32 v66, -1, v66
	v_permlane32_swap_b32_e32 v136, v137
	v_permlane32_swap_b32_e32 v133, v138
	v_permlane32_swap_b32_e32 v67, v68
	v_and_b32_e32 v86, 64, v66
	s_mov_b32 s14, 8
	s_mov_b32 s13, 0
	v_mov_b32_e32 v66, 0
	s_waitcnt lgkmcnt(0)
